# in-proj transposed-V epilogue rewritten: v_permlane16_swap pairs the two 8-byte token groups of neighbouring lane quarters so each lane issues one 16-byte store (16 dwordx4 instead of 32 dwordx2 per u
# baseline (speedup 1.0000x reference)
.LBB0_232:
	s_andn2_b64 vcc, exec, s[26:27]
	s_cbranch_vccnz .LBB0_219
	s_ashr_i32 s25, s17, 31
	s_lshr_b32 s25, s25, 21
	s_add_i32 s25, s17, s25
	s_and_b32 s25, s25, 0xfffff800
	v_lshrrev_b32_e32 v2, 4, v135
	s_sub_i32 s17, s17, s25
	s_lshl_b32 s25, s41, 2
	v_lshlrev_b32_e32 v132, 3, v134
	v_lshlrev_b32_e32 v2, 2, v2
	s_add_i32 s15, s15, s25
	v_and_b32_e32 v161, 16, v132
	v_lshl_add_u32 v132, v134, 5, s15
	s_ashr_i32 s15, s46, 31
	v_and_or_b32 v2, v2, 4, s17
	s_add_i32 s17, s44, s24
	ds_read_b128 v[144:147], v132
	ds_read_b128 v[140:143], v132 offset:16
	ds_read_b128 v[136:139], v132 offset:512
	ds_read_b128 v[132:135], v132 offset:528
	s_lshr_b32 s15, s15, 29
	v_or3_b32 v166, v2, v161, s41
	v_or_b32_e32 v2, s17, v160
	s_add_i32 s15, s46, s15
	v_add_u32_e32 v160, 0xfffffe80, v2
	v_ashrrev_i32_e32 v161, 31, v2
	v_cmp_gt_i32_e32 vcc, s93, v2
	s_ashr_i32 s15, s15, 3
	v_mov_b32_e32 v165, s3
	v_cndmask_b32_e32 v161, 0, v161, vcc
	v_cndmask_b32_e32 v160, v160, v2, vcc
	v_mov_b32_e32 v170, s1
	v_mov_b32_e32 v171, s2
	v_mov_b32_e32 v172, s0
	v_mad_i64_i32 v[160:161], s[24:25], s15, v226, v[160:161]
	v_ashrrev_i32_e32 v167, 31, v166
	v_cndmask_b32_e32 v169, v165, v170, vcc
	v_cndmask_b32_e32 v168, v171, v172, vcc
	v_lshlrev_b64 v[160:161], 12, v[160:161]
	v_lshl_add_u64 v[168:169], v[168:169], 0, v[160:161]
	v_lshlrev_b64 v[160:161], 1, v[166:167]
	s_waitcnt lgkmcnt(0)
	v_bfe_u32 v166, v162, 4, 1
	v_lshlrev_b32_e32 v166, 3, v166
	v_add_u32_e32 v160, v160, v166
	s_mul_i32 s100, s15, 0x180
	v_lshl_add_u64 v[168:169], v[168:169], 0, v[160:161]
	v_pk_mul_f32 v[128:129], v[128:129], v[144:145]
	v_pk_mul_f32 v[130:131], v[130:131], v[146:147]
	v_pk_mul_f32 v[124:125], v[124:125], v[140:141]
	v_pk_mul_f32 v[126:127], v[126:127], v[142:143]
	v_cvt_pk_bf16_f32 v128, v128, v129
	v_cvt_pk_bf16_f32 v129, v130, v131
	v_cvt_pk_bf16_f32 v130, v124, v125
	v_cvt_pk_bf16_f32 v131, v126, v127
	s_nop 1
	v_permlane16_swap_b32_e32 v128, v130
	v_permlane16_swap_b32_e32 v129, v131
	global_store_dwordx4 v[168:169], v[128:131], off
	v_pk_mul_f32 v[120:121], v[120:121], v[136:137]
	v_pk_mul_f32 v[122:123], v[122:123], v[138:139]
	v_pk_mul_f32 v[112:113], v[112:113], v[132:133]
	v_pk_mul_f32 v[114:115], v[114:115], v[134:135]
	v_cvt_pk_bf16_f32 v120, v120, v121
	v_cvt_pk_bf16_f32 v121, v122, v123
	v_cvt_pk_bf16_f32 v122, v112, v113
	v_cvt_pk_bf16_f32 v123, v114, v115
	s_nop 1
	v_permlane16_swap_b32_e32 v120, v122
	v_permlane16_swap_b32_e32 v121, v123
	global_store_dwordx4 v[168:169], v[120:123], off offset:256
	v_add_u32_e32 v166, 16, v2
	v_cmp_gt_i32_e32 vcc, s93, v166
	v_add_u32_e32 v167, 0xfffffe80, v166
	s_nop 1
	v_cndmask_b32_e32 v166, v167, v166, vcc
	v_cndmask_b32_e32 v169, v165, v170, vcc
	v_cndmask_b32_e32 v168, v171, v172, vcc
	v_add_u32_e32 v166, s100, v166
	v_mov_b32_e32 v167, 0
	v_lshlrev_b64 v[166:167], 12, v[166:167]
	v_lshl_add_u64 v[168:169], v[168:169], 0, v[166:167]
	v_lshl_add_u64 v[168:169], v[168:169], 0, v[160:161]
	v_pk_mul_f32 v[116:117], v[116:117], v[144:145]
	v_pk_mul_f32 v[118:119], v[118:119], v[146:147]
	v_pk_mul_f32 v[108:109], v[108:109], v[140:141]
	v_pk_mul_f32 v[110:111], v[110:111], v[142:143]
	v_cvt_pk_bf16_f32 v116, v116, v117
	v_cvt_pk_bf16_f32 v117, v118, v119
	v_cvt_pk_bf16_f32 v118, v108, v109
	v_cvt_pk_bf16_f32 v119, v110, v111
	s_nop 1
	v_permlane16_swap_b32_e32 v116, v118
	v_permlane16_swap_b32_e32 v117, v119
	global_store_dwordx4 v[168:169], v[116:119], off
	v_pk_mul_f32 v[104:105], v[104:105], v[136:137]
	v_pk_mul_f32 v[106:107], v[106:107], v[138:139]
	v_pk_mul_f32 v[96:97], v[96:97], v[132:133]
	v_pk_mul_f32 v[98:99], v[98:99], v[134:135]
	v_cvt_pk_bf16_f32 v104, v104, v105
	v_cvt_pk_bf16_f32 v105, v106, v107
	v_cvt_pk_bf16_f32 v106, v96, v97
	v_cvt_pk_bf16_f32 v107, v98, v99
	s_nop 1
	v_permlane16_swap_b32_e32 v104, v106
	v_permlane16_swap_b32_e32 v105, v107
	global_store_dwordx4 v[168:169], v[104:107], off offset:256
	v_add_u32_e32 v166, 32, v2
	v_cmp_gt_i32_e32 vcc, s93, v166
	v_add_u32_e32 v167, 0xfffffe80, v166
	s_nop 1
	v_cndmask_b32_e32 v166, v167, v166, vcc
	v_cndmask_b32_e32 v169, v165, v170, vcc
	v_cndmask_b32_e32 v168, v171, v172, vcc
	v_add_u32_e32 v166, s100, v166
	v_mov_b32_e32 v167, 0
	v_lshlrev_b64 v[166:167], 12, v[166:167]
	v_lshl_add_u64 v[168:169], v[168:169], 0, v[166:167]
	v_lshl_add_u64 v[168:169], v[168:169], 0, v[160:161]
	v_pk_mul_f32 v[100:101], v[100:101], v[144:145]
	v_pk_mul_f32 v[102:103], v[102:103], v[146:147]
	v_pk_mul_f32 v[92:93], v[92:93], v[140:141]
	v_pk_mul_f32 v[94:95], v[94:95], v[142:143]
	v_cvt_pk_bf16_f32 v100, v100, v101
	v_cvt_pk_bf16_f32 v101, v102, v103
	v_cvt_pk_bf16_f32 v102, v92, v93
	v_cvt_pk_bf16_f32 v103, v94, v95
	s_nop 1
	v_permlane16_swap_b32_e32 v100, v102
	v_permlane16_swap_b32_e32 v101, v103
	global_store_dwordx4 v[168:169], v[100:103], off
	v_pk_mul_f32 v[88:89], v[88:89], v[136:137]
	v_pk_mul_f32 v[90:91], v[90:91], v[138:139]
	v_pk_mul_f32 v[80:81], v[80:81], v[132:133]
	v_pk_mul_f32 v[82:83], v[82:83], v[134:135]
	v_cvt_pk_bf16_f32 v88, v88, v89
	v_cvt_pk_bf16_f32 v89, v90, v91
	v_cvt_pk_bf16_f32 v90, v80, v81
	v_cvt_pk_bf16_f32 v91, v82, v83
	s_nop 1
	v_permlane16_swap_b32_e32 v88, v90
	v_permlane16_swap_b32_e32 v89, v91
	global_store_dwordx4 v[168:169], v[88:91], off offset:256
	v_add_u32_e32 v166, 48, v2
	v_cmp_gt_i32_e32 vcc, s93, v166
	v_add_u32_e32 v167, 0xfffffe80, v166
	s_nop 1
	v_cndmask_b32_e32 v166, v167, v166, vcc
	v_cndmask_b32_e32 v169, v165, v170, vcc
	v_cndmask_b32_e32 v168, v171, v172, vcc
	v_add_u32_e32 v166, s100, v166
	v_mov_b32_e32 v167, 0
	v_lshlrev_b64 v[166:167], 12, v[166:167]
	v_lshl_add_u64 v[168:169], v[168:169], 0, v[166:167]
	v_lshl_add_u64 v[168:169], v[168:169], 0, v[160:161]
	v_pk_mul_f32 v[84:85], v[84:85], v[144:145]
	v_pk_mul_f32 v[86:87], v[86:87], v[146:147]
	v_pk_mul_f32 v[76:77], v[76:77], v[140:141]
	v_pk_mul_f32 v[78:79], v[78:79], v[142:143]
	v_cvt_pk_bf16_f32 v84, v84, v85
	v_cvt_pk_bf16_f32 v85, v86, v87
	v_cvt_pk_bf16_f32 v86, v76, v77
	v_cvt_pk_bf16_f32 v87, v78, v79
	s_nop 1
	v_permlane16_swap_b32_e32 v84, v86
	v_permlane16_swap_b32_e32 v85, v87
	global_store_dwordx4 v[168:169], v[84:87], off
	v_pk_mul_f32 v[72:73], v[72:73], v[136:137]
	v_pk_mul_f32 v[74:75], v[74:75], v[138:139]
	v_pk_mul_f32 v[68:69], v[68:69], v[132:133]
	v_pk_mul_f32 v[70:71], v[70:71], v[134:135]
	v_cvt_pk_bf16_f32 v72, v72, v73
	v_cvt_pk_bf16_f32 v73, v74, v75
	v_cvt_pk_bf16_f32 v74, v68, v69
	v_cvt_pk_bf16_f32 v75, v70, v71
	s_nop 1
	v_permlane16_swap_b32_e32 v72, v74
	v_permlane16_swap_b32_e32 v73, v75
	global_store_dwordx4 v[168:169], v[72:75], off offset:256
	v_add_u32_e32 v166, 128, v2
	v_cmp_gt_i32_e32 vcc, s93, v166
	v_add_u32_e32 v167, 0xfffffe80, v166
	s_nop 1
	v_cndmask_b32_e32 v166, v167, v166, vcc
	v_cndmask_b32_e32 v169, v165, v170, vcc
	v_cndmask_b32_e32 v168, v171, v172, vcc
	v_add_u32_e32 v166, s100, v166
	v_mov_b32_e32 v167, 0
	v_lshlrev_b64 v[166:167], 12, v[166:167]
	v_lshl_add_u64 v[168:169], v[168:169], 0, v[166:167]
	v_lshl_add_u64 v[168:169], v[168:169], 0, v[160:161]
	v_pk_mul_f32 v[64:65], v[64:65], v[144:145]
	v_pk_mul_f32 v[66:67], v[66:67], v[146:147]
	v_pk_mul_f32 v[60:61], v[60:61], v[140:141]
	v_pk_mul_f32 v[62:63], v[62:63], v[142:143]
	v_cvt_pk_bf16_f32 v64, v64, v65
	v_cvt_pk_bf16_f32 v65, v66, v67
	v_cvt_pk_bf16_f32 v66, v60, v61
	v_cvt_pk_bf16_f32 v67, v62, v63
	s_nop 1
	v_permlane16_swap_b32_e32 v64, v66
	v_permlane16_swap_b32_e32 v65, v67
	global_store_dwordx4 v[168:169], v[64:67], off
	v_pk_mul_f32 v[56:57], v[56:57], v[136:137]
	v_pk_mul_f32 v[58:59], v[58:59], v[138:139]
	v_pk_mul_f32 v[48:49], v[48:49], v[132:133]
	v_pk_mul_f32 v[50:51], v[50:51], v[134:135]
	v_cvt_pk_bf16_f32 v56, v56, v57
	v_cvt_pk_bf16_f32 v57, v58, v59
	v_cvt_pk_bf16_f32 v58, v48, v49
	v_cvt_pk_bf16_f32 v59, v50, v51
	s_nop 1
	v_permlane16_swap_b32_e32 v56, v58
	v_permlane16_swap_b32_e32 v57, v59
	global_store_dwordx4 v[168:169], v[56:59], off offset:256
	v_add_u32_e32 v166, 144, v2
	v_cmp_gt_i32_e32 vcc, s93, v166
	v_add_u32_e32 v167, 0xfffffe80, v166
	s_nop 1
	v_cndmask_b32_e32 v166, v167, v166, vcc
	v_cndmask_b32_e32 v169, v165, v170, vcc
	v_cndmask_b32_e32 v168, v171, v172, vcc
	v_add_u32_e32 v166, s100, v166
	v_mov_b32_e32 v167, 0
	v_lshlrev_b64 v[166:167], 12, v[166:167]
	v_lshl_add_u64 v[168:169], v[168:169], 0, v[166:167]
	v_lshl_add_u64 v[168:169], v[168:169], 0, v[160:161]
	v_pk_mul_f32 v[52:53], v[52:53], v[144:145]
	v_pk_mul_f32 v[54:55], v[54:55], v[146:147]
	v_pk_mul_f32 v[44:45], v[44:45], v[140:141]
	v_pk_mul_f32 v[46:47], v[46:47], v[142:143]
	v_cvt_pk_bf16_f32 v52, v52, v53
	v_cvt_pk_bf16_f32 v53, v54, v55
	v_cvt_pk_bf16_f32 v54, v44, v45
	v_cvt_pk_bf16_f32 v55, v46, v47
	s_nop 1
	v_permlane16_swap_b32_e32 v52, v54
	v_permlane16_swap_b32_e32 v53, v55
	global_store_dwordx4 v[168:169], v[52:55], off
	v_pk_mul_f32 v[40:41], v[40:41], v[136:137]
	v_pk_mul_f32 v[42:43], v[42:43], v[138:139]
	v_pk_mul_f32 v[32:33], v[32:33], v[132:133]
	v_pk_mul_f32 v[34:35], v[34:35], v[134:135]
	v_cvt_pk_bf16_f32 v40, v40, v41
	v_cvt_pk_bf16_f32 v41, v42, v43
	v_cvt_pk_bf16_f32 v42, v32, v33
	v_cvt_pk_bf16_f32 v43, v34, v35
	s_nop 1
	v_permlane16_swap_b32_e32 v40, v42
	v_permlane16_swap_b32_e32 v41, v43
	global_store_dwordx4 v[168:169], v[40:43], off offset:256
	v_add_u32_e32 v166, 160, v2
	v_cmp_gt_i32_e32 vcc, s93, v166
	v_add_u32_e32 v167, 0xfffffe80, v166
	s_nop 1
	v_cndmask_b32_e32 v166, v167, v166, vcc
	v_cndmask_b32_e32 v169, v165, v170, vcc
	v_cndmask_b32_e32 v168, v171, v172, vcc
	v_add_u32_e32 v166, s100, v166
	v_mov_b32_e32 v167, 0
	v_lshlrev_b64 v[166:167], 12, v[166:167]
	v_lshl_add_u64 v[168:169], v[168:169], 0, v[166:167]
	v_lshl_add_u64 v[168:169], v[168:169], 0, v[160:161]
	v_pk_mul_f32 v[36:37], v[36:37], v[144:145]
	v_pk_mul_f32 v[38:39], v[38:39], v[146:147]
	v_pk_mul_f32 v[28:29], v[28:29], v[140:141]
	v_pk_mul_f32 v[30:31], v[30:31], v[142:143]
	v_cvt_pk_bf16_f32 v36, v36, v37
	v_cvt_pk_bf16_f32 v37, v38, v39
	v_cvt_pk_bf16_f32 v38, v28, v29
	v_cvt_pk_bf16_f32 v39, v30, v31
	s_nop 1
	v_permlane16_swap_b32_e32 v36, v38
	v_permlane16_swap_b32_e32 v37, v39
	global_store_dwordx4 v[168:169], v[36:39], off
	v_pk_mul_f32 v[24:25], v[24:25], v[136:137]
	v_pk_mul_f32 v[26:27], v[26:27], v[138:139]
	v_pk_mul_f32 v[16:17], v[16:17], v[132:133]
	v_pk_mul_f32 v[18:19], v[18:19], v[134:135]
	v_cvt_pk_bf16_f32 v24, v24, v25
	v_cvt_pk_bf16_f32 v25, v26, v27
	v_cvt_pk_bf16_f32 v26, v16, v17
	v_cvt_pk_bf16_f32 v27, v18, v19
	s_nop 1
	v_permlane16_swap_b32_e32 v24, v26
	v_permlane16_swap_b32_e32 v25, v27
	global_store_dwordx4 v[168:169], v[24:27], off offset:256
	v_add_u32_e32 v166, 176, v2
	v_cmp_gt_i32_e32 vcc, s93, v166
	v_add_u32_e32 v167, 0xfffffe80, v166
	s_nop 1
	v_cndmask_b32_e32 v166, v167, v166, vcc
	v_cndmask_b32_e32 v169, v165, v170, vcc
	v_cndmask_b32_e32 v168, v171, v172, vcc
	v_add_u32_e32 v166, s100, v166
	v_mov_b32_e32 v167, 0
	v_lshlrev_b64 v[166:167], 12, v[166:167]
	v_lshl_add_u64 v[168:169], v[168:169], 0, v[166:167]
	v_lshl_add_u64 v[168:169], v[168:169], 0, v[160:161]
	v_pk_mul_f32 v[20:21], v[20:21], v[144:145]
	v_pk_mul_f32 v[22:23], v[22:23], v[146:147]
	v_pk_mul_f32 v[12:13], v[12:13], v[140:141]
	v_pk_mul_f32 v[14:15], v[14:15], v[142:143]
	v_cvt_pk_bf16_f32 v20, v20, v21
	v_cvt_pk_bf16_f32 v21, v22, v23
	v_cvt_pk_bf16_f32 v22, v12, v13
	v_cvt_pk_bf16_f32 v23, v14, v15
	s_nop 1
	v_permlane16_swap_b32_e32 v20, v22
	v_permlane16_swap_b32_e32 v21, v23
	global_store_dwordx4 v[168:169], v[20:23], off
	v_pk_mul_f32 v[8:9], v[8:9], v[136:137]
	v_pk_mul_f32 v[10:11], v[10:11], v[138:139]
	v_pk_mul_f32 v[4:5], v[4:5], v[132:133]
	v_pk_mul_f32 v[6:7], v[6:7], v[134:135]
	v_cvt_pk_bf16_f32 v8, v8, v9
	v_cvt_pk_bf16_f32 v9, v10, v11
	v_cvt_pk_bf16_f32 v10, v4, v5
	v_cvt_pk_bf16_f32 v11, v6, v7
	s_nop 1
	v_permlane16_swap_b32_e32 v8, v10
	v_permlane16_swap_b32_e32 v9, v11
	global_store_dwordx4 v[168:169], v[8:11], off offset:256
	s_branch .LBB0_219
